# MoE M3 units: dropped the per-wave L1 invalidate behind each flag poll (8 per CU per unit; no pre-final copy of H can exist in the reader's caches: see header comment of the change)
# speedup vs baseline: 1.0289x; 1.0289x over previous
.LBB0_1254:
	s_lshl_b32 s10, s12, 4
	s_add_u32 s2, s8, 0x59140000
	s_addc_u32 s3, s9, 0
	s_lshl_b32 s50, s90, 25
	s_lshl_b64 s[14:15], s[50:51], 2
	s_add_u32 s16, s6, s14
	s_addc_u32 s17, s7, s15
	v_and_b32_e32 v3, 60, v206
	s_add_i32 s22, 0, 0x24200
	v_add_u32_e32 v200, s22, v3
	v_ashrrev_i32_e32 v3, 2, v206
	v_and_b32_e32 v201, -16, v3
	v_lshl_add_u32 v3, v201, 2, v200
	ds_read_b32 v3, v3
	v_add_u32_e32 v7, 0x2000, v4
	v_ashrrev_i32_e32 v7, 6, v7
	v_and_b32_e32 v202, -16, v7
	v_lshl_add_u32 v7, v202, 2, v200
	s_ashr_i32 s6, s5, 6
	ds_read_b32 v7, v7
	s_lshl_b32 s13, s6, 10
	s_waitcnt lgkmcnt(1)
	v_max_i32_e32 v3, 0, v3
	v_and_b32_e32 v5, 32, v206
	v_and_b32_e32 v8, 48, v4
	v_lshlrev_b32_e32 v3, 10, v3
	s_add_i32 s13, s13, 0
	s_ashr_i32 s18, s5, 8
	s_and_b32 s19, s5, 0xc0
	v_bitop3_b32 v220, v3, v8, v5 bitop3:0xf6
	s_ashr_i32 s5, s4, 31
	s_mov_b32 m0, s13
	s_lshl_b32 s11, s18, 13
	s_lshl_b64 s[4:5], s[4:5], 22
	s_ashr_i32 s7, s6, 31
	global_load_lds_dwordx4 v220, s[2:3]
	s_add_i32 m0, s13, 0x2000
	s_waitcnt lgkmcnt(0)
	v_max_i32_e32 v3, 0, v7
	s_add_u32 s14, s16, s4
	v_lshlrev_b32_e32 v3, 10, v3
	v_lshlrev_b32_e32 v2, 8, v2
	s_addc_u32 s15, s17, s5
	s_lshl_b64 s[4:5], s[6:7], 13
	v_and_b32_e32 v1, 63, v206
	v_bitop3_b32 v221, v3, v8, v5 bitop3:0xf6
	v_ashrrev_i32_e32 v3, 31, v2
	s_add_u32 s6, s14, s4
	v_lshlrev_b32_e32 v0, 2, v1
	s_addc_u32 s7, s15, s5
	v_lshlrev_b64 v[2:3], 2, v[2:3]
	v_xor_b32_e32 v6, 16, v0
	v_lshl_add_u64 v[2:3], s[6:7], 0, v[2:3]
	global_load_lds_dwordx4 v221, s[2:3]
	v_lshlrev_b32_e32 v208, 4, v1
	v_lshlrev_b32_e32 v8, 2, v6
	v_mov_b32_e32 v9, v209
	s_add_i32 m0, s13, 0x4000
	v_readfirstlane_b32 s6, v2
	v_readfirstlane_b32 s7, v3
	v_lshl_add_u64 v[198:199], v[2:3], 0, v[8:9]
	v_lshl_add_u64 v[196:197], v[2:3], 0, v[208:209]
	v_or_b32_e32 v1, 64, v220
	v_lshlrev_b32_e32 v7, 2, v206
	v_and_b32_e32 v7, 32, v7
	global_load_lds_dwordx4 v208, s[6:7]
	s_mov_b64 s[6:7], 0x10000
	v_lshl_add_u64 v[2:3], v[198:199], 0, s[6:7]
	s_add_i32 m0, s13, 0x6000
	s_mov_b64 s[6:7], 0x20000
	global_load_lds_dwordx4 v[2:3], off
	v_lshl_add_u64 v[2:3], v[196:197], 0, s[6:7]
	s_add_i32 m0, s13, 0x8000
	s_mov_b64 s[6:7], 0x30000
	global_load_lds_dwordx4 v[2:3], off
	v_lshl_add_u64 v[2:3], v[198:199], 0, s[6:7]
	s_add_i32 m0, s13, 0xa000
	s_mov_b64 s[6:7], 0x40000
	global_load_lds_dwordx4 v[2:3], off
	s_add_i32 m0, s13, 0xc000
	v_lshl_add_u64 v[2:3], v[196:197], 0, s[6:7]
	global_load_lds_dwordx4 v1, s[2:3]
	v_or_b32_e32 v1, 64, v221
	s_add_i32 m0, s13, 0xe000
	s_mov_b64 s[6:7], 0x50000
	global_load_lds_dwordx4 v1, s[2:3]
	s_add_i32 m0, s13, 0x10000
	v_and_b32_e32 v1, 15, v206
	global_load_lds_dwordx4 v[2:3], off
	v_lshl_add_u64 v[2:3], v[198:199], 0, s[6:7]
	s_add_i32 m0, s13, 0x12000
	s_mov_b64 s[6:7], 0x60000
	global_load_lds_dwordx4 v[2:3], off
	v_lshl_add_u64 v[2:3], v[196:197], 0, s[6:7]
	s_add_i32 m0, s13, 0x14000
	s_mov_b64 s[6:7], 0x70000
	global_load_lds_dwordx4 v[2:3], off
	v_lshl_add_u64 v[2:3], v[198:199], 0, s[6:7]
	s_add_i32 m0, s13, 0x16000
	s_add_u32 s16, s16, s4
	global_load_lds_dwordx4 v[2:3], off
	v_lshlrev_b32_e32 v3, 6, v1
	v_and_b32_e32 v2, 48, v206
	v_bitop3_b32 v203, v3, v7, v2 bitop3:0x36
	v_lshlrev_b32_e32 v3, 1, v1
	v_and_b32_e32 v7, 16, v206
	s_addc_u32 s17, s17, s5
	s_lshl_b32 s7, s18, 9
	s_lshl_b32 s4, s19, 1
	v_bitop3_b32 v3, s19, v7, v3 bitop3:0x36
	s_add_u32 s4, s8, s4
	v_lshlrev_b32_e32 v205, 2, v3
	s_addc_u32 s5, s9, 0
	v_mov_b32_e32 v3, v209
	v_lshlrev_b32_e32 v7, 9, v206
	v_lshl_add_u64 v[2:3], s[4:5], 0, v[2:3]
	s_mov_b64 s[4:5], 0x5a140000
	s_add_i32 s22, s22, s7
	s_mov_b32 s6, 2
	s_mov_b32 s14, 16
	v_and_b32_e32 v204, 0x6000, v7
	v_bitop3_b32 v206, v4, v5, 48 bitop3:0x6c
	s_mov_b32 s15, 0
	v_lshl_add_u64 v[192:193], v[2:3], 0, s[4:5]
	v_lshl_add_u32 v207, v1, 2, s22
	v_lshlrev_b32_e32 v208, 2, v0
	v_lshlrev_b32_e32 v194, 2, v6
	s_mov_b32 s18, 2
	s_mov_b32 s19, 2
	s_mov_b32 s22, 0
	s_mov_b32 s23, 0
	s_mov_b32 s24, 0
	s_branch .LBB0_1256

.LBB0_1257:
	v_lshl_add_u32 v196, s15, 10, v200
	v_lshl_add_u32 v197, v201, 2, v196
	v_lshl_add_u32 v196, v202, 2, v196
	ds_read_b32 v197, v197
	ds_read_b32 v196, v196
	s_ashr_i32 s5, s4, 31
	s_lshl_b64 s[4:5], s[4:5], 22
	s_add_u32 s4, s16, s4
	s_waitcnt lgkmcnt(1)
	v_max_i32_e32 v197, 0, v197
	s_waitcnt lgkmcnt(0)
	v_max_i32_e32 v196, 0, v196
	v_lshl_or_b32 v221, v196, 10, v206
	v_lshlrev_b32_e32 v196, 8, v195
	v_lshl_or_b32 v220, v197, 10, v206
	v_ashrrev_i32_e32 v197, 31, v196
	s_addc_u32 s5, s17, s5
	v_lshlrev_b64 v[196:197], 2, v[196:197]
	v_lshl_add_u64 v[198:199], s[4:5], 0, v[196:197]
	v_mov_b32_e32 v195, v209
	v_lshl_add_u64 v[196:197], v[198:199], 0, v[208:209]
	v_lshl_add_u64 v[198:199], v[198:199], 0, v[194:195]
